# adds prep set-up load batching and norm1 (combine) load hoisting to the previous combined version
# baseline (speedup 1.0000x reference)
.LBB0_19:
	v_lshl_add_u64 v[54:55], v[32:33], 0, s[6:7]
	v_lshl_add_u64 v[56:57], v[30:31], 0, s[6:7]
	v_lshl_add_u64 v[58:59], v[28:29], 0, s[6:7]
	v_lshl_add_u64 v[60:61], v[26:27], 0, s[6:7]
	v_lshl_add_u64 v[62:63], v[24:25], 0, s[6:7]
	v_lshl_add_u64 v[64:65], v[22:23], 0, s[6:7]
	v_lshl_add_u64 v[66:67], v[20:21], 0, s[6:7]
	v_lshl_add_u64 v[68:69], v[18:19], 0, s[6:7]
	global_load_dword v53, v[54:55], off nt
	global_load_dword v53, v[54:55], off nt
	global_load_dword v70, v[56:57], off nt
	global_load_dword v70, v[56:57], off nt
	global_load_dword v71, v[58:59], off nt
	global_load_dword v71, v[58:59], off nt
	global_load_dword v72, v[60:61], off nt
	global_load_dword v72, v[60:61], off nt
	global_load_dword v73, v[62:63], off nt
	global_load_dword v73, v[62:63], off nt
	global_load_dword v74, v[64:65], off nt
	global_load_dword v74, v[64:65], off nt
	global_load_dword v75, v[66:67], off nt
	global_load_dword v75, v[66:67], off nt
	global_load_dword v76, v[68:69], off nt
	global_load_dword v76, v[68:69], off nt
	s_add_u32 s6, s6, 0x10000
	s_addc_u32 s7, s7, 0
	v_add_u32_e32 v54, 0x400, v52
	s_cmp_lg_u32 s6, 0x40000
	s_waitcnt vmcnt(7)
	v_mul_f32_e32 v53, 0x42800000, v53
	s_waitcnt vmcnt(6)
	v_mul_f32_e32 v55, 0x42800000, v70
	s_waitcnt vmcnt(5)
	v_mul_f32_e32 v56, 0x42800000, v71
	s_waitcnt vmcnt(4)
	v_mul_f32_e32 v57, 0x42800000, v72
	s_waitcnt vmcnt(3)
	v_mul_f32_e32 v58, 0x42800000, v73
	s_waitcnt vmcnt(2)
	v_mul_f32_e32 v59, 0x42800000, v74
	s_waitcnt vmcnt(1)
	v_mul_f32_e32 v60, 0x42800000, v75
	s_waitcnt vmcnt(0)
	v_mul_f32_e32 v61, 0x42800000, v76
	ds_write2_b32 v52, v53, v55 offset1:66
	ds_write2_b32 v52, v56, v57 offset0:132 offset1:198
	ds_write2_b32 v54, v58, v59 offset0:8 offset1:74
	ds_write2_b32 v54, v60, v61 offset0:140 offset1:206
	v_add_u32_e32 v52, 0x840, v52
	s_cbranch_scc1 .LBB0_19
	s_waitcnt lgkmcnt(0)
	ds_read2_b32 v[22:23], v37 offset0:66 offset1:99
	ds_read2_b32 v[18:19], v37 offset1:33
	v_mov_b32_e32 v24, 0x43e00000
	s_add_i32 s2, s17, 0xfffde000
	s_waitcnt lgkmcnt(1)
	v_med3_f32 v26, v22, -v24, v24
	v_med3_f32 v27, v23, -v24, v24
	ds_read2_b32 v[22:23], v37 offset0:132 offset1:165
	s_waitcnt lgkmcnt(1)
	v_med3_f32 v25, v18, -v24, v24
	v_med3_f32 v19, v19, -v24, v24
	v_mov_b32_e32 v18, v3
	v_cvt_pk_fp8_f32 v18, v25, v19
	ds_read2_b32 v[24:25], v37 offset0:198 offset1:231
	v_mov_b32_e32 v28, 0x43e00000
	s_lshr_b32 s2, s2, 9
	v_mov_b32_e32 v19, v3
	s_waitcnt lgkmcnt(1)
	v_med3_f32 v22, v22, -v28, v28
	v_med3_f32 v23, v23, -v28, v28
	s_lshl_b64 s[6:7], s[2:3], 20
	s_lshl_b32 s2, s17, 1
	s_lshl_b32 s12, s17, 5
	v_cvt_pk_fp8_f32 v19, v22, v23
	s_and_b32 s2, s2, 0x3c0
	s_and_b32 s12, s12, 0x3e0
	s_add_u32 s6, s19, s6
	s_addc_u32 s7, s20, s7
	s_waitcnt lgkmcnt(0)
	v_med3_f32 v22, v24, -v28, v28
	v_med3_f32 v23, v25, -v28, v28
	s_add_u32 s6, s6, s2
	v_cvt_pk_fp8_f32 v18, v26, v27 op_sel:[0,0,1]
	v_cvt_pk_fp8_f32 v19, v22, v23 op_sel:[0,0,1]
	s_addc_u32 s7, s7, 0
	v_or_b32_e32 v22, s12, v36
	v_lshl_add_u64 v[20:21], s[6:7], 0, v[0:1]
	v_lshlrev_b32_e32 v22, 10, v22
	v_mov_b32_e32 v23, v3
	v_lshl_add_u64 v[22:23], v[20:21], 0, v[22:23]
	ds_read2_b32 v[24:25], v37 offset0:8 offset1:41
	global_store_dwordx2 v[22:23], v[18:19], off
	ds_read2_b32 v[18:19], v37 offset0:74 offset1:107
	v_mov_b32_e32 v22, 0x43e00000
	v_mov_b32_e32 v28, 0x43e00000
	s_waitcnt lgkmcnt(1)
	v_med3_f32 v24, v24, -v22, v22
	v_med3_f32 v25, v25, -v22, v22
	s_waitcnt lgkmcnt(0)
	v_med3_f32 v26, v18, -v22, v22
	v_med3_f32 v27, v19, -v22, v22
	ds_read2_b32 v[22:23], v37 offset0:140 offset1:173
	v_mov_b32_e32 v18, v3
	v_cvt_pk_fp8_f32 v18, v24, v25
	ds_read2_b32 v[24:25], v37 offset0:206 offset1:239
	v_mov_b32_e32 v19, v3
	s_waitcnt lgkmcnt(1)
	v_med3_f32 v22, v22, -v28, v28
	v_med3_f32 v23, v23, -v28, v28
	v_cvt_pk_fp8_f32 v19, v22, v23
	s_waitcnt lgkmcnt(0)
	v_med3_f32 v22, v24, -v28, v28
	v_med3_f32 v23, v25, -v28, v28
	v_cvt_pk_fp8_f32 v18, v26, v27 op_sel:[0,0,1]
	v_cvt_pk_fp8_f32 v19, v22, v23 op_sel:[0,0,1]
	v_or_b32_e32 v22, s12, v38
	v_lshlrev_b32_e32 v22, 10, v22
	v_mov_b32_e32 v23, v3
	v_lshl_add_u64 v[22:23], v[20:21], 0, v[22:23]
	ds_read2_b32 v[24:25], v37 offset0:16 offset1:49
	global_store_dwordx2 v[22:23], v[18:19], off
	ds_read2_b32 v[18:19], v37 offset0:82 offset1:115
	v_mov_b32_e32 v22, 0x43e00000
	v_mov_b32_e32 v28, 0x43e00000
	s_waitcnt lgkmcnt(1)
	v_med3_f32 v24, v24, -v22, v22
	v_med3_f32 v25, v25, -v22, v22
	s_waitcnt lgkmcnt(0)
	v_med3_f32 v26, v18, -v22, v22
	v_med3_f32 v27, v19, -v22, v22
	ds_read2_b32 v[22:23], v37 offset0:148 offset1:181
	v_mov_b32_e32 v18, v3
	v_cvt_pk_fp8_f32 v18, v24, v25
	ds_read2_b32 v[24:25], v37 offset0:214 offset1:247
	v_mov_b32_e32 v19, v3
	s_waitcnt lgkmcnt(1)
	v_med3_f32 v22, v22, -v28, v28
	v_med3_f32 v23, v23, -v28, v28
	v_cvt_pk_fp8_f32 v19, v22, v23
	s_waitcnt lgkmcnt(0)
	v_med3_f32 v22, v24, -v28, v28
	v_med3_f32 v23, v25, -v28, v28
	v_cvt_pk_fp8_f32 v18, v26, v27 op_sel:[0,0,1]
	v_cvt_pk_fp8_f32 v19, v22, v23 op_sel:[0,0,1]
	v_or_b32_e32 v22, s12, v39
	v_lshlrev_b32_e32 v22, 10, v22
	v_mov_b32_e32 v23, v3
	v_lshl_add_u64 v[22:23], v[20:21], 0, v[22:23]
	ds_read2_b32 v[24:25], v37 offset0:24 offset1:57
	global_store_dwordx2 v[22:23], v[18:19], off
	ds_read2_b32 v[18:19], v37 offset0:90 offset1:123
	v_mov_b32_e32 v22, 0x43e00000
	v_mov_b32_e32 v28, 0x43e00000
	s_waitcnt lgkmcnt(1)
	v_med3_f32 v24, v24, -v22, v22
	v_med3_f32 v25, v25, -v22, v22
	s_waitcnt lgkmcnt(0)
	v_med3_f32 v26, v18, -v22, v22
	v_med3_f32 v27, v19, -v22, v22
	ds_read2_b32 v[22:23], v37 offset0:156 offset1:189
	v_mov_b32_e32 v18, v3
	v_cvt_pk_fp8_f32 v18, v24, v25
	ds_read2_b32 v[24:25], v37 offset0:222 offset1:255
	v_mov_b32_e32 v19, v3
	s_waitcnt lgkmcnt(1)
	v_med3_f32 v22, v22, -v28, v28
	v_med3_f32 v23, v23, -v28, v28
	v_cvt_pk_fp8_f32 v19, v22, v23
	s_waitcnt lgkmcnt(0)
	v_med3_f32 v22, v24, -v28, v28
	v_med3_f32 v23, v25, -v28, v28
	v_cvt_pk_fp8_f32 v18, v26, v27 op_sel:[0,0,1]
	v_cvt_pk_fp8_f32 v19, v22, v23 op_sel:[0,0,1]
	v_or_b32_e32 v22, s12, v40
	v_lshlrev_b32_e32 v22, 10, v22
	v_mov_b32_e32 v23, v3
	v_lshl_add_u64 v[20:21], v[20:21], 0, v[22:23]
	global_store_dwordx2 v[20:21], v[18:19], off
	s_waitcnt lgkmcnt(0)
	s_mov_b64 s[6:7], 0

.LBB0_23:
	v_lshl_add_u64 v[54:55], v[32:33], 0, s[6:7]
	v_lshl_add_u64 v[56:57], v[30:31], 0, s[6:7]
	v_lshl_add_u64 v[58:59], v[28:29], 0, s[6:7]
	v_lshl_add_u64 v[60:61], v[26:27], 0, s[6:7]
	v_lshl_add_u64 v[62:63], v[24:25], 0, s[6:7]
	v_lshl_add_u64 v[64:65], v[22:23], 0, s[6:7]
	v_lshl_add_u64 v[66:67], v[20:21], 0, s[6:7]
	v_lshl_add_u64 v[68:69], v[18:19], 0, s[6:7]
	global_load_dword v53, v[54:55], off nt
	global_load_dword v53, v[54:55], off nt
	global_load_dword v70, v[56:57], off nt
	global_load_dword v70, v[56:57], off nt
	global_load_dword v71, v[58:59], off nt
	global_load_dword v71, v[58:59], off nt
	global_load_dword v72, v[60:61], off nt
	global_load_dword v72, v[60:61], off nt
	global_load_dword v73, v[62:63], off nt
	global_load_dword v73, v[62:63], off nt
	global_load_dword v74, v[64:65], off nt
	global_load_dword v74, v[64:65], off nt
	global_load_dword v75, v[66:67], off nt
	global_load_dword v75, v[66:67], off nt
	global_load_dword v76, v[68:69], off nt
	global_load_dword v76, v[68:69], off nt
	s_add_u32 s6, s6, 0x20000
	s_addc_u32 s7, s7, 0
	v_add_u32_e32 v54, 0x400, v52
	s_cmp_lg_u32 s6, 0x80000
	s_waitcnt vmcnt(7)
	v_mul_f32_e32 v53, 0x42800000, v53
	s_waitcnt vmcnt(6)
	v_mul_f32_e32 v55, 0x42800000, v70
	s_waitcnt vmcnt(5)
	v_mul_f32_e32 v56, 0x42800000, v71
	s_waitcnt vmcnt(4)
	v_mul_f32_e32 v57, 0x42800000, v72
	s_waitcnt vmcnt(3)
	v_mul_f32_e32 v58, 0x42800000, v73
	s_waitcnt vmcnt(2)
	v_mul_f32_e32 v59, 0x42800000, v74
	s_waitcnt vmcnt(1)
	v_mul_f32_e32 v60, 0x42800000, v75
	s_waitcnt vmcnt(0)
	v_mul_f32_e32 v61, 0x42800000, v76
	ds_write2_b32 v52, v53, v55 offset1:66
	ds_write2_b32 v52, v56, v57 offset0:132 offset1:198
	ds_write2_b32 v54, v58, v59 offset0:8 offset1:74
	ds_write2_b32 v54, v60, v61 offset0:140 offset1:206
	v_add_u32_e32 v52, 0x840, v52
	s_cbranch_scc1 .LBB0_23
	s_waitcnt lgkmcnt(0)
	ds_read2_b32 v[22:23], v37 offset0:66 offset1:99
	ds_read2_b32 v[18:19], v37 offset1:33
	v_mov_b32_e32 v24, 0x43e00000
	s_add_i32 s2, s17, 0xffffe000
	s_waitcnt lgkmcnt(1)
	v_med3_f32 v26, v22, -v24, v24
	v_med3_f32 v27, v23, -v24, v24
	ds_read2_b32 v[22:23], v37 offset0:132 offset1:165
	s_waitcnt lgkmcnt(1)
	v_med3_f32 v25, v18, -v24, v24
	v_med3_f32 v19, v19, -v24, v24
	v_mov_b32_e32 v18, v3
	v_cvt_pk_fp8_f32 v18, v25, v19
	ds_read2_b32 v[24:25], v37 offset0:198 offset1:231
	v_mov_b32_e32 v28, 0x43e00000
	s_lshr_b32 s2, s2, 10
	v_mov_b32_e32 v19, v3
	s_waitcnt lgkmcnt(1)
	v_med3_f32 v22, v22, -v28, v28
	v_med3_f32 v23, v23, -v28, v28
	s_lshl_b64 s[6:7], s[2:3], 21
	v_cvt_pk_fp8_f32 v19, v22, v23
	s_add_u32 s2, s21, s6
	s_addc_u32 s7, s22, s7
	s_lshl_b32 s6, s17, 5
	s_and_b32 s13, s6, 0x7e0
	s_waitcnt lgkmcnt(0)
	v_med3_f32 v22, v24, -v28, v28
	v_med3_f32 v23, v25, -v28, v28
	s_add_u32 s6, s2, s12
	v_cvt_pk_fp8_f32 v18, v26, v27 op_sel:[0,0,1]
	v_cvt_pk_fp8_f32 v19, v22, v23 op_sel:[0,0,1]
	s_addc_u32 s7, s7, 0
	v_or_b32_e32 v22, s13, v36
	v_lshl_add_u64 v[20:21], s[6:7], 0, v[0:1]
	v_lshlrev_b32_e32 v22, 10, v22
	v_mov_b32_e32 v23, v3
	v_lshl_add_u64 v[22:23], v[20:21], 0, v[22:23]
	ds_read2_b32 v[24:25], v37 offset0:8 offset1:41
	global_store_dwordx2 v[22:23], v[18:19], off
	ds_read2_b32 v[18:19], v37 offset0:74 offset1:107
	v_mov_b32_e32 v22, 0x43e00000
	v_mov_b32_e32 v28, 0x43e00000
	s_waitcnt lgkmcnt(1)
	v_med3_f32 v24, v24, -v22, v22
	v_med3_f32 v25, v25, -v22, v22
	s_waitcnt lgkmcnt(0)
	v_med3_f32 v26, v18, -v22, v22
	v_med3_f32 v27, v19, -v22, v22
	ds_read2_b32 v[22:23], v37 offset0:140 offset1:173
	v_mov_b32_e32 v18, v3
	v_cvt_pk_fp8_f32 v18, v24, v25
	ds_read2_b32 v[24:25], v37 offset0:206 offset1:239
	v_mov_b32_e32 v19, v3
	s_waitcnt lgkmcnt(1)
	v_med3_f32 v22, v22, -v28, v28
	v_med3_f32 v23, v23, -v28, v28
	v_cvt_pk_fp8_f32 v19, v22, v23
	s_waitcnt lgkmcnt(0)
	v_med3_f32 v22, v24, -v28, v28
	v_med3_f32 v23, v25, -v28, v28
	v_cvt_pk_fp8_f32 v18, v26, v27 op_sel:[0,0,1]
	v_cvt_pk_fp8_f32 v19, v22, v23 op_sel:[0,0,1]
	v_or_b32_e32 v22, s13, v38
	v_lshlrev_b32_e32 v22, 10, v22
	v_mov_b32_e32 v23, v3
	v_lshl_add_u64 v[22:23], v[20:21], 0, v[22:23]
	ds_read2_b32 v[24:25], v37 offset0:16 offset1:49
	global_store_dwordx2 v[22:23], v[18:19], off
	ds_read2_b32 v[18:19], v37 offset0:82 offset1:115
	v_mov_b32_e32 v22, 0x43e00000
	v_mov_b32_e32 v28, 0x43e00000
	s_waitcnt lgkmcnt(1)
	v_med3_f32 v24, v24, -v22, v22
	v_med3_f32 v25, v25, -v22, v22
	s_waitcnt lgkmcnt(0)
	v_med3_f32 v26, v18, -v22, v22
	v_med3_f32 v27, v19, -v22, v22
	ds_read2_b32 v[22:23], v37 offset0:148 offset1:181
	v_mov_b32_e32 v18, v3
	v_cvt_pk_fp8_f32 v18, v24, v25
	ds_read2_b32 v[24:25], v37 offset0:214 offset1:247
	v_mov_b32_e32 v19, v3
	s_waitcnt lgkmcnt(1)
	v_med3_f32 v22, v22, -v28, v28
	v_med3_f32 v23, v23, -v28, v28
	v_cvt_pk_fp8_f32 v19, v22, v23
	s_waitcnt lgkmcnt(0)
	v_med3_f32 v22, v24, -v28, v28
	v_med3_f32 v23, v25, -v28, v28
	v_cvt_pk_fp8_f32 v18, v26, v27 op_sel:[0,0,1]
	v_cvt_pk_fp8_f32 v19, v22, v23 op_sel:[0,0,1]
	v_or_b32_e32 v22, s13, v39
	v_lshlrev_b32_e32 v22, 10, v22
	v_mov_b32_e32 v23, v3
	v_lshl_add_u64 v[22:23], v[20:21], 0, v[22:23]
	ds_read2_b32 v[24:25], v37 offset0:24 offset1:57
	global_store_dwordx2 v[22:23], v[18:19], off
	ds_read2_b32 v[18:19], v37 offset0:90 offset1:123
	v_mov_b32_e32 v22, 0x43e00000
	v_mov_b32_e32 v28, 0x43e00000
	s_waitcnt lgkmcnt(1)
	v_med3_f32 v24, v24, -v22, v22
	v_med3_f32 v25, v25, -v22, v22
	s_waitcnt lgkmcnt(0)
	v_med3_f32 v26, v18, -v22, v22
	v_med3_f32 v27, v19, -v22, v22
	ds_read2_b32 v[22:23], v37 offset0:156 offset1:189
	v_mov_b32_e32 v18, v3
	v_cvt_pk_fp8_f32 v18, v24, v25
	ds_read2_b32 v[24:25], v37 offset0:222 offset1:255
	v_mov_b32_e32 v19, v3
	s_waitcnt lgkmcnt(1)
	v_med3_f32 v22, v22, -v28, v28
	v_med3_f32 v23, v23, -v28, v28
	v_cvt_pk_fp8_f32 v19, v22, v23
	s_waitcnt lgkmcnt(0)
	v_med3_f32 v22, v24, -v28, v28
	v_med3_f32 v23, v25, -v28, v28
	v_cvt_pk_fp8_f32 v18, v26, v27 op_sel:[0,0,1]
	v_cvt_pk_fp8_f32 v19, v22, v23 op_sel:[0,0,1]
	v_or_b32_e32 v22, s13, v40
	v_lshlrev_b32_e32 v22, 10, v22
	v_mov_b32_e32 v23, v3
	v_lshl_add_u64 v[20:21], v[20:21], 0, v[22:23]
	global_store_dwordx2 v[20:21], v[18:19], off
	s_waitcnt lgkmcnt(0)

.LBB0_28:
	v_lshl_add_u64 v[20:21], v[18:19], 0, s[6:7]
	v_lshl_add_u64 v[22:23], v[16:17], 0, s[6:7]
	v_lshl_add_u64 v[24:25], v[14:15], 0, s[6:7]
	v_lshl_add_u64 v[26:27], v[12:13], 0, s[6:7]
	v_lshl_add_u64 v[28:29], v[10:11], 0, s[6:7]
	v_lshl_add_u64 v[30:31], v[8:9], 0, s[6:7]
	v_lshl_add_u64 v[32:33], v[6:7], 0, s[6:7]
	v_lshl_add_u64 v[52:53], v[4:5], 0, s[6:7]
	global_load_dword v51, v[20:21], off nt
	global_load_dword v51, v[20:21], off nt
	global_load_dword v54, v[22:23], off nt
	global_load_dword v54, v[22:23], off nt
	global_load_dword v55, v[24:25], off nt
	global_load_dword v55, v[24:25], off nt
	global_load_dword v56, v[26:27], off nt
	global_load_dword v56, v[26:27], off nt
	global_load_dword v57, v[28:29], off nt
	global_load_dword v57, v[28:29], off nt
	global_load_dword v58, v[30:31], off nt
	global_load_dword v58, v[30:31], off nt
	global_load_dword v59, v[32:33], off nt
	global_load_dword v59, v[32:33], off nt
	global_load_dword v60, v[52:53], off nt
	global_load_dword v60, v[52:53], off nt
	s_add_u32 s6, s6, 0x10000
	s_addc_u32 s7, s7, 0
	v_add_u32_e32 v20, 0x400, v2
	s_cmp_lg_u32 s6, 0x40000
	s_waitcnt vmcnt(7)
	v_mul_f32_e32 v21, 0x42800000, v51
	s_waitcnt vmcnt(6)
	v_mul_f32_e32 v22, 0x42800000, v54
	s_waitcnt vmcnt(5)
	v_mul_f32_e32 v23, 0x42800000, v55
	s_waitcnt vmcnt(4)
	v_mul_f32_e32 v24, 0x42800000, v56
	s_waitcnt vmcnt(3)
	v_mul_f32_e32 v25, 0x42800000, v57
	s_waitcnt vmcnt(2)
	v_mul_f32_e32 v26, 0x42800000, v58
	s_waitcnt vmcnt(1)
	v_mul_f32_e32 v27, 0x42800000, v59
	s_waitcnt vmcnt(0)
	v_mul_f32_e32 v28, 0x42800000, v60
	ds_write2_b32 v2, v21, v22 offset1:66
	ds_write2_b32 v2, v23, v24 offset0:132 offset1:198
	ds_write2_b32 v20, v25, v26 offset0:8 offset1:74
	ds_write2_b32 v20, v27, v28 offset0:140 offset1:206
	v_add_u32_e32 v2, 0x840, v2
	s_cbranch_scc1 .LBB0_28
	s_waitcnt lgkmcnt(0)
	ds_read2_b32 v[4:5], v37 offset1:33
	ds_read2_b32 v[8:9], v37 offset0:66 offset1:99
	v_mov_b32_e32 v2, 0x43e00000
	s_add_i32 s2, s17, 0xffffe800
	s_waitcnt lgkmcnt(1)
	v_med3_f32 v10, v4, -v2, v2
	v_med3_f32 v5, v5, -v2, v2
	s_waitcnt lgkmcnt(0)
	v_med3_f32 v12, v8, -v2, v2
	v_med3_f32 v2, v9, -v2, v2
	ds_read2_b32 v[8:9], v37 offset0:132 offset1:165
	v_mov_b32_e32 v4, v3
	v_cvt_pk_fp8_f32 v4, v10, v5
	ds_read2_b32 v[10:11], v37 offset0:198 offset1:231
	v_mov_b32_e32 v13, 0x43e00000
	s_lshr_b32 s2, s2, 9
	v_mov_b32_e32 v5, v3
	s_waitcnt lgkmcnt(1)
	v_med3_f32 v8, v8, -v13, v13
	v_med3_f32 v9, v9, -v13, v13
	s_lshl_b64 s[6:7], s[2:3], 20
	s_lshl_b32 s2, s17, 1
	s_lshl_b32 s12, s17, 5
	v_cvt_pk_fp8_f32 v5, v8, v9
	s_and_b32 s2, s2, 0x3c0
	s_and_b32 s12, s12, 0x3e0
	s_add_u32 s6, s23, s6
	s_addc_u32 s7, s24, s7
	v_cvt_pk_fp8_f32 v4, v12, v2 op_sel:[0,0,1]
	s_waitcnt lgkmcnt(0)
	v_med3_f32 v2, v10, -v13, v13
	v_med3_f32 v8, v11, -v13, v13
	s_add_u32 s6, s6, s2
	v_cvt_pk_fp8_f32 v5, v2, v8 op_sel:[0,0,1]
	s_addc_u32 s7, s7, 0
	v_or_b32_e32 v2, s12, v36
	v_lshl_add_u64 v[6:7], s[6:7], 0, v[0:1]
	v_lshlrev_b32_e32 v2, 10, v2
	v_lshl_add_u64 v[8:9], v[6:7], 0, v[2:3]
	ds_read2_b32 v[10:11], v37 offset0:8 offset1:41
	global_store_dwordx2 v[8:9], v[4:5], off
	ds_read2_b32 v[4:5], v37 offset0:74 offset1:107
	v_mov_b32_e32 v2, 0x43e00000
	ds_read2_b32 v[8:9], v37 offset0:140 offset1:173
	s_waitcnt lgkmcnt(2)
	v_med3_f32 v10, v10, -v2, v2
	v_med3_f32 v11, v11, -v2, v2
	s_waitcnt lgkmcnt(1)
	v_med3_f32 v12, v4, -v2, v2
	v_mov_b32_e32 v4, v3
	v_cvt_pk_fp8_f32 v4, v10, v11
	ds_read2_b32 v[10:11], v37 offset0:206 offset1:239
	v_mov_b32_e32 v13, 0x43e00000
	v_med3_f32 v2, v5, -v2, v2
	v_mov_b32_e32 v5, v3
	s_waitcnt lgkmcnt(1)
	v_med3_f32 v8, v8, -v13, v13
	v_med3_f32 v9, v9, -v13, v13
	v_cvt_pk_fp8_f32 v5, v8, v9
	v_cvt_pk_fp8_f32 v4, v12, v2 op_sel:[0,0,1]
	s_waitcnt lgkmcnt(0)
	v_med3_f32 v2, v10, -v13, v13
	v_med3_f32 v8, v11, -v13, v13
	v_cvt_pk_fp8_f32 v5, v2, v8 op_sel:[0,0,1]
	v_or_b32_e32 v2, s12, v38
	v_lshlrev_b32_e32 v2, 10, v2
	v_lshl_add_u64 v[8:9], v[6:7], 0, v[2:3]
	ds_read2_b32 v[10:11], v37 offset0:16 offset1:49
	global_store_dwordx2 v[8:9], v[4:5], off
	ds_read2_b32 v[4:5], v37 offset0:82 offset1:115
	v_mov_b32_e32 v2, 0x43e00000
	ds_read2_b32 v[8:9], v37 offset0:148 offset1:181
	s_waitcnt lgkmcnt(2)
	v_med3_f32 v10, v10, -v2, v2
	v_med3_f32 v11, v11, -v2, v2
	s_waitcnt lgkmcnt(1)
	v_med3_f32 v12, v4, -v2, v2
	v_mov_b32_e32 v4, v3
	v_cvt_pk_fp8_f32 v4, v10, v11
	ds_read2_b32 v[10:11], v37 offset0:214 offset1:247
	v_mov_b32_e32 v13, 0x43e00000
	v_med3_f32 v2, v5, -v2, v2
	v_mov_b32_e32 v5, v3
	s_waitcnt lgkmcnt(1)
	v_med3_f32 v8, v8, -v13, v13
	v_med3_f32 v9, v9, -v13, v13
	v_cvt_pk_fp8_f32 v5, v8, v9
	v_cvt_pk_fp8_f32 v4, v12, v2 op_sel:[0,0,1]
	s_waitcnt lgkmcnt(0)
	v_med3_f32 v2, v10, -v13, v13
	v_med3_f32 v8, v11, -v13, v13
	v_cvt_pk_fp8_f32 v5, v2, v8 op_sel:[0,0,1]
	v_or_b32_e32 v2, s12, v39
	v_lshlrev_b32_e32 v2, 10, v2
	v_lshl_add_u64 v[8:9], v[6:7], 0, v[2:3]
	ds_read2_b32 v[10:11], v37 offset0:24 offset1:57
	global_store_dwordx2 v[8:9], v[4:5], off
	ds_read2_b32 v[4:5], v37 offset0:90 offset1:123
	v_mov_b32_e32 v2, 0x43e00000
	ds_read2_b32 v[8:9], v37 offset0:156 offset1:189
	s_waitcnt lgkmcnt(2)
	v_med3_f32 v10, v10, -v2, v2
	v_med3_f32 v11, v11, -v2, v2
	s_waitcnt lgkmcnt(1)
	v_med3_f32 v12, v4, -v2, v2
	v_mov_b32_e32 v4, v3
	v_cvt_pk_fp8_f32 v4, v10, v11
	ds_read2_b32 v[10:11], v37 offset0:222 offset1:255
	v_mov_b32_e32 v13, 0x43e00000
	v_med3_f32 v2, v5, -v2, v2
	v_mov_b32_e32 v5, v3
	s_waitcnt lgkmcnt(1)
	v_med3_f32 v8, v8, -v13, v13
	v_med3_f32 v9, v9, -v13, v13
	v_cvt_pk_fp8_f32 v5, v8, v9
	v_cvt_pk_fp8_f32 v4, v12, v2 op_sel:[0,0,1]
	s_waitcnt lgkmcnt(0)
	v_med3_f32 v2, v10, -v13, v13
	v_med3_f32 v8, v11, -v13, v13
	v_cvt_pk_fp8_f32 v5, v2, v8 op_sel:[0,0,1]
	v_or_b32_e32 v2, s12, v40
	v_lshlrev_b32_e32 v2, 10, v2
	v_lshl_add_u64 v[6:7], v[6:7], 0, v[2:3]
	global_store_dwordx2 v[6:7], v[4:5], off
	s_waitcnt lgkmcnt(0)

.LBB0_62:
	s_or_b64 exec, exec, s[12:13]
	s_sext_i32_i16 s12, s41
	s_lshl_b32 s14, s12, 6
	v_cmp_lt_i32_e32 vcc, -1, v2
	v_lshlrev_b64 v[18:19], 2, v[2:3]
	v_or_b32_e32 v2, s14, v44
	v_mul_hi_i32_i24_e32 v7, 0x2ca0, v2
	v_mul_i32_i24_e32 v6, 0x2ca0, v2
	v_or_b32_e32 v2, s14, v45
	v_mul_hi_i32_i24_e32 v9, 0x2ca0, v2
	v_mul_i32_i24_e32 v8, 0x2ca0, v2
	v_or_b32_e32 v2, s14, v46
	v_mul_hi_i32_i24_e32 v11, 0x2ca0, v2
	v_mul_i32_i24_e32 v10, 0x2ca0, v2
	v_or_b32_e32 v2, s14, v47
	v_mul_hi_i32_i24_e32 v13, 0x2ca0, v2
	v_mul_i32_i24_e32 v12, 0x2ca0, v2
	v_or_b32_e32 v2, s14, v48
	v_mul_hi_i32_i24_e32 v15, 0x2ca0, v2
	v_mul_i32_i24_e32 v14, 0x2ca0, v2
	v_or_b32_e32 v2, s14, v49
	v_or_b32_e32 v4, s14, v43
	v_mul_hi_i32_i24_e32 v17, 0x2ca0, v2
	v_mul_i32_i24_e32 v16, 0x2ca0, v2
	v_or_b32_e32 v2, s14, v35
	v_mul_hi_i32_i24_e32 v5, 0x2ca0, v4
	v_mul_i32_i24_e32 v4, 0x2ca0, v4
	v_mul_hi_i32_i24_e32 v21, 0x2ca0, v2
	v_mul_i32_i24_e32 v20, 0x2ca0, v2
	v_mad_i64_i32 v[4:5], s[12:13], s40, v50, v[4:5]
	v_mad_i64_i32 v[6:7], s[12:13], s40, v50, v[6:7]
	v_mad_i64_i32 v[8:9], s[12:13], s40, v50, v[8:9]
	v_mad_i64_i32 v[10:11], s[12:13], s40, v50, v[10:11]
	v_mad_i64_i32 v[12:13], s[12:13], s40, v50, v[12:13]
	v_mad_i64_i32 v[14:15], s[12:13], s40, v50, v[14:15]
	v_mad_i64_i32 v[16:17], s[12:13], s40, v50, v[16:17]
	v_mad_i64_i32 v[20:21], s[12:13], s40, v50, v[20:21]
	v_lshl_add_u64 v[4:5], v[4:5], 0, v[18:19]
	v_lshl_add_u64 v[6:7], v[6:7], 0, v[18:19]
	v_lshl_add_u64 v[8:9], v[8:9], 0, v[18:19]
	v_lshl_add_u64 v[10:11], v[10:11], 0, v[18:19]
	v_lshl_add_u64 v[12:13], v[12:13], 0, v[18:19]
	v_lshl_add_u64 v[14:15], v[14:15], 0, v[18:19]
	v_lshl_add_u64 v[16:17], v[16:17], 0, v[18:19]
	v_lshl_add_u64 v[18:19], v[20:21], 0, v[18:19]
	s_waitcnt lgkmcnt(0)
	v_lshl_add_u64 v[4:5], s[6:7], 0, v[4:5]
	v_lshl_add_u64 v[6:7], s[6:7], 0, v[6:7]
	v_lshl_add_u64 v[8:9], s[6:7], 0, v[8:9]
	v_lshl_add_u64 v[10:11], s[6:7], 0, v[10:11]
	v_lshl_add_u64 v[12:13], s[6:7], 0, v[12:13]
	v_lshl_add_u64 v[14:15], s[6:7], 0, v[14:15]
	v_lshl_add_u64 v[16:17], s[6:7], 0, v[16:17]
	v_lshl_add_u64 v[18:19], s[6:7], 0, v[18:19]
	s_mov_b64 s[6:7], 0
	v_mov_b32_e32 v2, v41
	s_branch .LBB0_64
.LBB0_63:
	s_or_b64 exec, exec, s[12:13]
	s_add_u32 s6, s6, 0x2ca00
	s_addc_u32 s7, s7, 0
	ds_write_b32 v2, v20 offset:1848
	s_cmp_lg_u32 s6, 0xb2800
	v_add_u32_e32 v2, 0x840, v2
	s_cbranch_scc0 .LBB0_13
.LBB0_64:
	v_mov_b32_e32 v20, 0
	v_mov_b32_e32 v21, 0
	s_and_saveexec_b64 s[12:13], vcc
	s_cbranch_execz .LBB0_66
	v_lshl_add_u64 v[22:23], v[18:19], 0, s[6:7]
	global_load_dword v21, v[22:23], off nt
	s_waitcnt vmcnt(0)
	v_mul_f32_e32 v21, 0x42800000, v21
.LBB0_66:
	s_or_b64 exec, exec, s[12:13]
	ds_write_b32 v2, v21
	s_and_saveexec_b64 s[12:13], vcc
	s_cbranch_execz .LBB0_68
	v_lshl_add_u64 v[20:21], v[16:17], 0, s[6:7]
	global_load_dword v20, v[20:21], off nt
	s_waitcnt vmcnt(0)
	v_mul_f32_e32 v20, 0x42800000, v20
.LBB0_68:
	s_or_b64 exec, exec, s[12:13]
	ds_write_b32 v2, v20 offset:264
	v_mov_b32_e32 v20, 0
	v_mov_b32_e32 v21, 0
	s_and_saveexec_b64 s[12:13], vcc
	s_cbranch_execz .LBB0_70
	v_lshl_add_u64 v[22:23], v[14:15], 0, s[6:7]
	global_load_dword v21, v[22:23], off nt
	s_waitcnt vmcnt(0)
	v_mul_f32_e32 v21, 0x42800000, v21
.LBB0_70:
	s_or_b64 exec, exec, s[12:13]
	ds_write_b32 v2, v21 offset:528
	s_and_saveexec_b64 s[12:13], vcc
	s_cbranch_execz .LBB0_72
	v_lshl_add_u64 v[20:21], v[12:13], 0, s[6:7]
	global_load_dword v20, v[20:21], off nt
	s_waitcnt vmcnt(0)
	v_mul_f32_e32 v20, 0x42800000, v20
.LBB0_72:
	s_or_b64 exec, exec, s[12:13]
	ds_write_b32 v2, v20 offset:792
	v_mov_b32_e32 v20, 0
	v_mov_b32_e32 v21, 0
	s_and_saveexec_b64 s[12:13], vcc
	s_cbranch_execz .LBB0_74
	v_lshl_add_u64 v[22:23], v[10:11], 0, s[6:7]
	global_load_dword v21, v[22:23], off nt
	s_waitcnt vmcnt(0)
	v_mul_f32_e32 v21, 0x42800000, v21
.LBB0_74:
	s_or_b64 exec, exec, s[12:13]
	ds_write_b32 v2, v21 offset:1056
	s_and_saveexec_b64 s[12:13], vcc
	s_cbranch_execz .LBB0_76
	v_lshl_add_u64 v[20:21], v[8:9], 0, s[6:7]
	global_load_dword v20, v[20:21], off nt
	s_waitcnt vmcnt(0)
	v_mul_f32_e32 v20, 0x42800000, v20
.LBB0_76:
	s_or_b64 exec, exec, s[12:13]
	ds_write_b32 v2, v20 offset:1320
	v_mov_b32_e32 v20, 0
	v_mov_b32_e32 v21, 0
	s_and_saveexec_b64 s[12:13], vcc
	s_cbranch_execz .LBB0_78
	v_lshl_add_u64 v[22:23], v[6:7], 0, s[6:7]
	global_load_dword v21, v[22:23], off nt
	s_waitcnt vmcnt(0)
	v_mul_f32_e32 v21, 0x42800000, v21
.LBB0_78:
	s_or_b64 exec, exec, s[12:13]
	ds_write_b32 v2, v21 offset:1584
	s_and_saveexec_b64 s[12:13], vcc
	s_cbranch_execz .LBB0_63
	v_lshl_add_u64 v[20:21], v[4:5], 0, s[6:7]
	global_load_dword v20, v[20:21], off nt
	s_waitcnt vmcnt(0)
	v_mul_f32_e32 v20, 0x42800000, v20
	s_branch .LBB0_63

.LBB0_97:
	v_lshl_add_u32 v87, s12, 7, v59
	v_add_u32_e32 v56, v87, v60
	v_ashrrev_i32_e32 v57, 31, v56
	v_add_u32_e32 v88, v87, v62
	v_add_u32_e32 v90, v87, v63
	v_add_u32_e32 v92, v87, v64
	v_add_u32_e32 v94, v87, v65
	v_add_u32_e32 v96, v87, v66
	v_add_u32_e32 v98, v87, v67
	v_add_u32_e32 v100, v87, v68
	v_lshl_add_u64 v[56:57], v[56:57], 2, s[4:5]
	v_ashrrev_i32_e32 v89, 31, v88
	v_ashrrev_i32_e32 v91, 31, v90
	v_ashrrev_i32_e32 v93, 31, v92
	v_ashrrev_i32_e32 v95, 31, v94
	v_ashrrev_i32_e32 v97, 31, v96
	v_ashrrev_i32_e32 v99, 31, v98
	v_ashrrev_i32_e32 v101, 31, v100
	s_barrier
	v_lshl_add_u64 v[88:89], v[88:89], 2, s[4:5]
	v_lshl_add_u64 v[90:91], v[90:91], 2, s[4:5]
	v_lshl_add_u64 v[92:93], v[92:93], 2, s[4:5]
	v_lshl_add_u64 v[94:95], v[94:95], 2, s[4:5]
	v_lshl_add_u64 v[96:97], v[96:97], 2, s[4:5]
	v_lshl_add_u64 v[98:99], v[98:99], 2, s[4:5]
	v_lshl_add_u64 v[100:101], v[100:101], 2, s[4:5]
	global_load_dword v87, v[56:57], off
	global_load_dword v102, v[88:89], off
	global_load_dword v103, v[90:91], off
	global_load_dword v104, v[92:93], off
	global_load_dword v105, v[94:95], off
	global_load_dword v106, v[96:97], off
	global_load_dword v107, v[98:99], off
	global_load_dword v108, v[100:101], off
	s_mov_b32 s15, 0
	s_waitcnt vmcnt(7)
	v_mul_f32_e32 v56, 0xbfb8aa3b, v87
	s_waitcnt vmcnt(6)
	v_mul_f32_e32 v57, 0xbfb8aa3b, v102
	s_waitcnt vmcnt(5)
	v_mul_f32_e32 v88, 0xbfb8aa3b, v103
	s_waitcnt vmcnt(4)
	v_mul_f32_e32 v89, 0xbfb8aa3b, v104
	s_waitcnt vmcnt(3)
	v_mul_f32_e32 v90, 0xbfb8aa3b, v105
	s_waitcnt vmcnt(2)
	v_mul_f32_e32 v91, 0xbfb8aa3b, v106
	s_waitcnt vmcnt(1)
	v_mul_f32_e32 v92, 0xbfb8aa3b, v107
	s_waitcnt vmcnt(0)
	v_mul_f32_e32 v93, 0xbfb8aa3b, v108
	v_exp_f32_e32 v56, v56
	v_exp_f32_e32 v57, v57
	v_exp_f32_e32 v88, v88
	v_exp_f32_e32 v89, v89
	v_exp_f32_e32 v90, v90
	v_exp_f32_e32 v91, v91
	v_exp_f32_e32 v92, v92
	v_exp_f32_e32 v93, v93
	v_add_f32_e32 v56, 1.0, v56
	v_add_f32_e32 v57, 1.0, v57
	v_add_f32_e32 v88, 1.0, v88
	v_add_f32_e32 v89, 1.0, v89
	v_add_f32_e32 v90, 1.0, v90
	v_add_f32_e32 v91, 1.0, v91
	v_add_f32_e32 v92, 1.0, v92
	v_add_f32_e32 v93, 1.0, v93
	v_rcp_f32_e32 v56, v56
	v_rcp_f32_e32 v57, v57
	v_rcp_f32_e32 v88, v88
	v_rcp_f32_e32 v89, v89
	v_rcp_f32_e32 v90, v90
	v_rcp_f32_e32 v91, v91
	v_rcp_f32_e32 v92, v92
	v_rcp_f32_e32 v93, v93
	v_mul_f32_e32 v56, v87, v56
	v_mul_f32_e32 v57, v102, v57
	v_mul_f32_e32 v87, v103, v88
	v_mul_f32_e32 v88, v104, v89
	v_mul_f32_e32 v89, v105, v90
	v_mul_f32_e32 v90, v106, v91
	v_mul_f32_e32 v91, v107, v92
	v_mul_f32_e32 v92, v108, v93
	ds_write2st64_b32 v61, v56, v57 offset1:8
	ds_write2st64_b32 v61, v87, v88 offset0:16 offset1:24
	ds_write2st64_b32 v61, v89, v90 offset0:32 offset1:40
	ds_write2st64_b32 v61, v91, v92 offset0:48 offset1:56
	v_mov_b64_e32 v[56:57], v[22:23]
	s_waitcnt lgkmcnt(0)
	s_barrier
.LBB0_98:
	global_load_dword v104, v[56:57], off
	v_add_u32_e32 v87, s15, v85
	ds_read_b128 v[88:91], v87
	ds_read_b128 v[92:95], v87 offset:16
	ds_read_b128 v[96:99], v87 offset:32
	ds_read_b128 v[100:103], v87 offset:48
	s_addk_i32 s15, 0x100
	s_cmpk_eq_i32 s15, 0x1000
	s_waitcnt vmcnt(0) lgkmcnt(3)
	v_pk_fma_f32 v[88:89], v[104:105], v[88:89], v[24:25] op_sel_hi:[0,1,1]
	v_pk_fma_f32 v[90:91], v[104:105], v[90:91], v[26:27] op_sel_hi:[0,1,1]
	ds_read_b128 v[24:27], v87 offset:64
	s_waitcnt lgkmcnt(3)
	v_pk_fma_f32 v[92:93], v[104:105], v[92:93], v[28:29] op_sel_hi:[0,1,1]
	v_pk_fma_f32 v[94:95], v[104:105], v[94:95], v[30:31] op_sel_hi:[0,1,1]
	ds_read_b128 v[28:31], v87 offset:144
	s_waitcnt lgkmcnt(3)
	v_pk_fma_f32 v[96:97], v[104:105], v[96:97], v[32:33] op_sel_hi:[0,1,1]
	s_waitcnt lgkmcnt(1)
	v_pk_fma_f32 v[106:107], v[104:105], v[24:25], v[40:41] op_sel_hi:[0,1,1]
	v_pk_fma_f32 v[108:109], v[104:105], v[26:27], v[42:43] op_sel_hi:[0,1,1]
	ds_read_b128 v[24:27], v87 offset:80
	v_pk_fma_f32 v[98:99], v[104:105], v[98:99], v[34:35] op_sel_hi:[0,1,1]
	ds_read_b128 v[32:35], v87 offset:160
	v_pk_fma_f32 v[100:101], v[104:105], v[100:101], v[36:37] op_sel_hi:[0,1,1]
	v_pk_fma_f32 v[102:103], v[104:105], v[102:103], v[38:39] op_sel_hi:[0,1,1]
	s_waitcnt lgkmcnt(1)
	v_pk_fma_f32 v[110:111], v[104:105], v[24:25], v[44:45] op_sel_hi:[0,1,1]
	v_pk_fma_f32 v[112:113], v[104:105], v[26:27], v[46:47] op_sel_hi:[0,1,1]
	ds_read_b128 v[24:27], v87 offset:96
	ds_read_b128 v[36:39], v87 offset:176
	ds_read_b128 v[40:43], v87 offset:192
	ds_read_b128 v[44:47], v87 offset:208
	s_waitcnt lgkmcnt(3)
	v_pk_fma_f32 v[114:115], v[104:105], v[24:25], v[48:49] op_sel_hi:[0,1,1]
	v_pk_fma_f32 v[116:117], v[104:105], v[26:27], v[50:51] op_sel_hi:[0,1,1]
	ds_read_b128 v[24:27], v87 offset:112
	ds_read_b128 v[48:51], v87 offset:224
	s_waitcnt lgkmcnt(1)
	v_pk_fma_f32 v[118:119], v[104:105], v[24:25], v[52:53] op_sel_hi:[0,1,1]
	v_add_co_u32_e32 v24, vcc, s14, v56
	v_pk_fma_f32 v[104:105], v[104:105], v[26:27], v[54:55] op_sel_hi:[0,1,1]
	s_nop 0
	v_addc_co_u32_e32 v25, vcc, 0, v57, vcc
	global_load_dword v120, v[24:25], off
	ds_read_b128 v[24:27], v87 offset:128
	ds_read_b128 v[52:55], v87 offset:240
	v_lshl_add_u64 v[56:57], v[56:57], 0, s[6:7]
	s_waitcnt vmcnt(0) lgkmcnt(1)
	v_pk_fma_f32 v[24:25], v[120:121], v[24:25], v[88:89] op_sel_hi:[0,1,1]
	v_pk_fma_f32 v[26:27], v[120:121], v[26:27], v[90:91] op_sel_hi:[0,1,1]
	v_pk_fma_f32 v[28:29], v[120:121], v[28:29], v[92:93] op_sel_hi:[0,1,1]
	v_pk_fma_f32 v[30:31], v[120:121], v[30:31], v[94:95] op_sel_hi:[0,1,1]
	v_pk_fma_f32 v[32:33], v[120:121], v[32:33], v[96:97] op_sel_hi:[0,1,1]
	v_pk_fma_f32 v[34:35], v[120:121], v[34:35], v[98:99] op_sel_hi:[0,1,1]
	v_pk_fma_f32 v[36:37], v[120:121], v[36:37], v[100:101] op_sel_hi:[0,1,1]
	v_pk_fma_f32 v[38:39], v[120:121], v[38:39], v[102:103] op_sel_hi:[0,1,1]
	v_pk_fma_f32 v[40:41], v[120:121], v[40:41], v[106:107] op_sel_hi:[0,1,1]
	v_pk_fma_f32 v[42:43], v[120:121], v[42:43], v[108:109] op_sel_hi:[0,1,1]
	v_pk_fma_f32 v[44:45], v[120:121], v[44:45], v[110:111] op_sel_hi:[0,1,1]
	v_pk_fma_f32 v[46:47], v[120:121], v[46:47], v[112:113] op_sel_hi:[0,1,1]
	v_pk_fma_f32 v[48:49], v[120:121], v[48:49], v[114:115] op_sel_hi:[0,1,1]
	v_pk_fma_f32 v[50:51], v[120:121], v[50:51], v[116:117] op_sel_hi:[0,1,1]
	s_waitcnt lgkmcnt(0)
	v_pk_fma_f32 v[52:53], v[120:121], v[52:53], v[118:119] op_sel_hi:[0,1,1]
	v_pk_fma_f32 v[54:55], v[120:121], v[54:55], v[104:105] op_sel_hi:[0,1,1]
	s_cbranch_scc0 .LBB0_98
	s_add_i32 s12, s12, 1
	s_cmp_eq_u32 s12, 8
	v_lshl_add_u64 v[22:23], v[22:23], 0, s[8:9]
	s_cbranch_scc0 .LBB0_97
	s_mul_i32 s12, s10, 48
	s_sub_i32 s12, s0, s12
	s_lshl_b32 s12, s12, 7
	s_add_i32 s13, s13, s12
	v_or_b32_e32 v22, s13, v58
	v_ashrrev_i32_e32 v23, 31, v22
	v_lshl_add_u64 v[22:23], v[22:23], 2, s[2:3]
	ds_write2st64_b32 v69, v24, v25 offset0:128 offset1:130
	ds_write2st64_b32 v69, v26, v27 offset0:132 offset1:134
	ds_write2st64_b32 v69, v28, v29 offset0:136 offset1:138
	ds_write2st64_b32 v69, v30, v31 offset0:140 offset1:142
	ds_write2st64_b32 v69, v32, v33 offset0:144 offset1:146
	ds_write2st64_b32 v69, v34, v35 offset0:148 offset1:150
	ds_write2st64_b32 v69, v36, v37 offset0:152 offset1:154
	ds_write2st64_b32 v69, v38, v39 offset0:156 offset1:158
	ds_write2st64_b32 v69, v40, v41 offset0:160 offset1:162
	ds_write2st64_b32 v69, v42, v43 offset0:164 offset1:166
	ds_write2st64_b32 v69, v44, v45 offset0:168 offset1:170
	ds_write2st64_b32 v69, v46, v47 offset0:172 offset1:174
	ds_write2st64_b32 v69, v48, v49 offset0:176 offset1:178
	ds_write2st64_b32 v69, v50, v51 offset0:180 offset1:182
	ds_write2st64_b32 v69, v52, v53 offset0:184 offset1:186
	ds_write2st64_b32 v69, v54, v55 offset0:188 offset1:190
	s_waitcnt lgkmcnt(0)
	s_barrier
	global_load_dword v34, v[22:23], off
	ds_read2st64_b32 v[24:25], v61 offset0:128 offset1:136
	ds_read2st64_b32 v[26:27], v71 offset0:128 offset1:192
	ds_read_b32 v32, v70 offset:49152
	ds_read_b32 v35, v72 offset:49152
	ds_read_b32 v36, v74 offset:49152
	ds_read_b32 v37, v76 offset:49152
	ds_read_b32 v38, v78 offset:49152
	ds_read_b32 v39, v80 offset:49152
	ds_read_b32 v40, v82 offset:49152
	ds_read_b32 v41, v2 offset:49152
	s_lshl_b64 s[10:11], s[10:11], 5
	s_ashr_i32 s13, s12, 31
	s_waitcnt lgkmcnt(7)
	v_add_f32_e32 v24, v24, v32
	v_lshl_add_u64 v[28:29], s[10:11], 0, v[0:1]
	v_lshl_add_u64 v[30:31], s[12:13], 2, v[4:5]
	v_add_f32_e32 v24, v24, v26
	v_mad_u64_u32 v[32:33], s[12:13], v28, s14, v[30:31]
	v_add_f32_e32 v24, v24, v27
	v_mad_i32_i24 v33, v29, s14, v33
	ds_read2st64_b32 v[26:27], v73 offset0:128 offset1:192
	v_lshl_add_u64 v[28:29], s[10:11], 0, v[6:7]
	s_add_i32 s0, s0, s1
	s_cmpk_gt_i32 s0, 0xbf
	s_waitcnt vmcnt(0)
	v_add_f32_e32 v24, v24, v34
	global_store_dword v[32:33], v24, off
	global_load_dword v32, v[22:23], off
	s_waitcnt lgkmcnt(7)
	v_add_f32_e32 v33, v25, v35
	s_waitcnt lgkmcnt(0)
	v_add_f32_e32 v26, v33, v26
	v_mad_u64_u32 v[24:25], s[12:13], v28, s14, v[30:31]
	v_add_f32_e32 v26, v26, v27
	v_mad_i32_i24 v25, v29, s14, v25
	v_lshl_add_u64 v[28:29], s[10:11], 0, v[8:9]
	s_waitcnt vmcnt(0)
	v_add_f32_e32 v26, v26, v32
	global_store_dword v[24:25], v26, off
	global_load_dword v34, v[22:23], off
	ds_read2st64_b32 v[24:25], v61 offset0:144 offset1:152
	ds_read2st64_b32 v[26:27], v75 offset0:128 offset1:192
	v_mad_u64_u32 v[32:33], s[12:13], v28, s14, v[30:31]
	v_mad_i32_i24 v33, v29, s14, v33
	s_waitcnt lgkmcnt(1)
	v_add_f32_e32 v24, v24, v36
	s_waitcnt lgkmcnt(0)
	v_add_f32_e32 v24, v24, v26
	v_add_f32_e32 v24, v24, v27
	ds_read2st64_b32 v[26:27], v77 offset0:128 offset1:192
	v_lshl_add_u64 v[28:29], s[10:11], 0, v[10:11]
	s_waitcnt vmcnt(0)
	v_add_f32_e32 v24, v24, v34
	global_store_dword v[32:33], v24, off
	global_load_dword v32, v[22:23], off
	v_add_f32_e32 v33, v25, v37
	s_waitcnt lgkmcnt(0)
	v_add_f32_e32 v26, v33, v26
	v_mad_u64_u32 v[24:25], s[12:13], v28, s14, v[30:31]
	v_add_f32_e32 v26, v26, v27
	v_mad_i32_i24 v25, v29, s14, v25
	v_lshl_add_u64 v[28:29], s[10:11], 0, v[12:13]
	s_waitcnt vmcnt(0)
	v_add_f32_e32 v26, v26, v32
	global_store_dword v[24:25], v26, off
	global_load_dword v34, v[22:23], off
	ds_read2st64_b32 v[24:25], v61 offset0:160 offset1:168
	ds_read2st64_b32 v[26:27], v79 offset0:128 offset1:192
	v_mad_u64_u32 v[32:33], s[12:13], v28, s14, v[30:31]
	v_mad_i32_i24 v33, v29, s14, v33
	s_waitcnt lgkmcnt(1)
	v_add_f32_e32 v24, v24, v38
	s_waitcnt lgkmcnt(0)
	v_add_f32_e32 v24, v24, v26
	v_add_f32_e32 v24, v24, v27
	ds_read2st64_b32 v[26:27], v81 offset0:128 offset1:192
	v_lshl_add_u64 v[28:29], s[10:11], 0, v[14:15]
	s_waitcnt vmcnt(0)
	v_add_f32_e32 v24, v24, v34
	global_store_dword v[32:33], v24, off
	global_load_dword v32, v[22:23], off
	v_add_f32_e32 v33, v25, v39
	s_waitcnt lgkmcnt(0)
	v_add_f32_e32 v26, v33, v26
	v_mad_u64_u32 v[24:25], s[12:13], v28, s14, v[30:31]
	v_add_f32_e32 v26, v26, v27
	v_mad_i32_i24 v25, v29, s14, v25
	v_lshl_add_u64 v[28:29], s[10:11], 0, v[16:17]
	s_waitcnt vmcnt(0)
	v_add_f32_e32 v26, v26, v32
	global_store_dword v[24:25], v26, off
	global_load_dword v34, v[22:23], off
	ds_read2st64_b32 v[24:25], v61 offset0:176 offset1:184
	ds_read2st64_b32 v[26:27], v83 offset0:128 offset1:192
	v_mad_u64_u32 v[32:33], s[12:13], v28, s14, v[30:31]
	v_mad_i32_i24 v33, v29, s14, v33
	s_waitcnt lgkmcnt(1)
	v_add_f32_e32 v24, v24, v40
	s_waitcnt lgkmcnt(0)
	v_add_f32_e32 v24, v24, v26
	v_add_f32_e32 v24, v24, v27
	v_add_f32_e32 v29, v25, v41
	v_lshl_add_u64 v[26:27], s[10:11], 0, v[18:19]
	s_waitcnt vmcnt(0)
	v_add_f32_e32 v24, v24, v34
	global_store_dword v[32:33], v24, off
	global_load_dword v28, v[22:23], off
	ds_read2st64_b32 v[22:23], v84 offset0:128 offset1:192
	v_mad_u64_u32 v[24:25], s[10:11], v26, s14, v[30:31]
	v_mad_i32_i24 v25, v27, s14, v25
	s_waitcnt lgkmcnt(0)
	v_add_f32_e32 v22, v29, v22
	v_add_f32_e32 v22, v22, v23
	s_waitcnt vmcnt(0)
	v_add_f32_e32 v22, v22, v28
	global_store_dword v[24:25], v22, off
	s_barrier
	s_cbranch_scc0 .LBB0_96
